# E row loop: nt loads for the once-read y and fp16 residual rows
# speedup vs baseline: 1.0153x; 1.0106x over previous
.LBB0_949:
	v_lshl_add_u64 v[80:81], v[68:69], 0, v[116:117]
	v_mov_b64_e32 v[68:69], v[96:97]
	s_and_b64 vcc, exec, s[42:43]
	v_mov_b64_e32 v[70:71], v[98:99]
	s_cbranch_vccnz .LBB0_951
	global_load_dwordx4 v[68:71], v[80:81], off offset:2048 nt
.LBB0_951:
	s_ashr_i32 s29, s28, 31
	s_lshl_b64 s[28:29], s[28:29], 11
	v_mov_b64_e32 v[72:73], v[88:89]
	v_lshl_add_u64 v[166:167], v[104:105], 0, s[28:29]
	s_and_b64 vcc, exec, s[44:45]
	v_mov_b64_e32 v[74:75], v[90:91]
	s_cbranch_vccnz .LBB0_953
	global_load_dwordx4 v[72:75], v[166:167], off nt
.LBB0_953:
	v_mov_b64_e32 v[76:77], v[92:93]
	s_and_b64 vcc, exec, s[42:43]
	v_mov_b64_e32 v[78:79], v[94:95]
	s_cbranch_vccnz .LBB0_955
	global_load_dwordx4 v[76:79], v[80:81], off offset:3072 nt
.LBB0_955:
	v_mov_b64_e32 v[80:81], v[84:85]
	s_and_b64 vcc, exec, s[44:45]
	v_mov_b64_e32 v[82:83], v[86:87]
	s_cbranch_vccnz .LBB0_957
	global_load_dwordx4 v[80:83], v[166:167], off offset:1024 nt
